# priority alternation switched exactly at the in-loop barrier (waves 4-7 first) and one tile later (waves 0-3)
# speedup vs baseline: 1.0029x; 1.0029x over previous
.LBB0_734:
	s_waitcnt lgkmcnt(6)
	v_mfma_f32_16x16x32_bf16 v[64:67], v[160:163], v[96:99], 0
	v_exp_f32_e32 v88, v88
	v_mfma_f32_16x16x32_bf16 v[68:71], v[160:163], v[112:115], 0
	v_exp_f32_e32 v92, v92
	ds_read_b128 v[234:237], v209 offset:6144
	s_add_u32 s16, s22, s10
	s_addc_u32 s17, s23, s11
	s_add_u32 s15, s22, s12
	s_addc_u32 s14, s23, s13
	s_add_u32 s8, s16, 0x3bc00200
	s_addc_u32 s9, s17, 0
	s_add_u32 s6, s15, 0x23a50000
	s_addc_u32 s7, s14, 0
	s_waitcnt lgkmcnt(6)
	v_mfma_f32_16x16x32_bf16 v[0:3], v[164:167], v[216:219], v[0:3]
	v_cvt_pk_bf16_f32 v242, v80, v81
	v_mfma_f32_16x16x32_bf16 v[4:7], v[164:167], v[238:241], v[4:7]
	v_exp_f32_e32 v89, v89
	ds_read_b128 v[160:163], v201 offset:20480
	s_waitcnt vmcnt(4)
	ds_write_b128 v225, v[152:155] offset:49152
	s_waitcnt lgkmcnt(7)
	v_mfma_f32_16x16x32_bf16 v[68:71], v[168:171], v[116:119], v[68:71]
	v_exp_f32_e32 v93, v93
	v_mfma_f32_16x16x32_bf16 v[64:67], v[168:171], v[100:103], v[64:67]
	v_cvt_pk_bf16_f32 v243, v82, v83
	ds_read_b128 v[164:167], v209 offset:8192
	ds_write_b128 v226, v[156:159] offset:49152
	s_waitcnt lgkmcnt(8)
	v_mfma_f32_16x16x32_bf16 v[12:15], v[172:175], v[238:241], v[12:15]
	v_exp_f32_e32 v90, v90
	v_mfma_f32_16x16x32_bf16 v[8:11], v[172:175], v[216:219], v[8:11]
	v_exp_f32_e32 v94, v94
	ds_read_b128 v[168:171], v202 offset:20480
	ds_write_b64 v227, v[132:133] offset:32768
	s_waitcnt lgkmcnt(9)
	v_mfma_f32_16x16x32_bf16 v[64:67], v[176:179], v[104:107], v[64:67]
	v_cvt_pk_bf16_f32 v204, v84, v85
	v_mfma_f32_16x16x32_bf16 v[68:71], v[176:179], v[120:123], v[68:71]
	v_exp_f32_e32 v91, v91
	ds_read_b128 v[172:175], v209 offset:10240
	ds_write_b64 v228, v[134:135] offset:32768
	s_waitcnt lgkmcnt(10)
	v_mfma_f32_16x16x32_bf16 v[16:19], v[180:183], v[216:219], v[16:19]
	v_exp_f32_e32 v95, v95
	v_mfma_f32_16x16x32_bf16 v[20:23], v[180:183], v[238:241], v[20:23]
	v_cvt_pk_bf16_f32 v205, v86, v87
	v_add_f32_e32 v220, v220, v88
	ds_read_b128 v[176:179], v203 offset:20480
	ds_write_b64 v229, v[128:129] offset:32768
	s_waitcnt lgkmcnt(11)
	v_mfma_f32_16x16x32_bf16 v[68:71], v[230:233], v[124:127], v[68:71]
	v_add_f32_e32 v221, v221, v92
	v_add_f32_e32 v220, v220, v89
	v_mfma_f32_16x16x32_bf16 v[64:67], v[230:233], v[108:111], v[64:67]
	v_add_f32_e32 v221, v221, v93
	v_cvt_pk_bf16_f32 v244, v88, v89
	ds_read_b128 v[180:183], v209 offset:12288
	ds_write_b64 v184, v[130:131] offset:32768
	s_waitcnt lgkmcnt(12)
	v_mfma_f32_16x16x32_bf16 v[28:31], v[234:237], v[238:241], v[28:31]
	v_cvt_pk_bf16_f32 v245, v90, v91
	v_cvt_pk_bf16_f32 v206, v92, v93
	v_mfma_f32_16x16x32_bf16 v[24:27], v[234:237], v[216:219], v[24:27]
	v_cvt_pk_bf16_f32 v207, v94, v95
	ds_read_b128 v[230:233], v246 offset:20480
	global_load_dwordx4 v[132:135], v198, s[8:9]
	s_waitcnt lgkmcnt(12)
	v_mfma_f32_16x16x32_bf16 v[72:75], v[160:163], v[96:99], 0
	v_add_f32_e32 v220, v220, v90
	v_add_f32_e32 v221, v221, v94
	v_mfma_f32_16x16x32_bf16 v[76:79], v[160:163], v[112:115], 0
	v_add_f32_e32 v220, v220, v91
	v_add_f32_e32 v221, v221, v95
	ds_read_b128 v[234:237], v209 offset:14336
	global_load_dwordx4 v[128:131], v199, s[8:9]
	s_waitcnt lgkmcnt(11)
	v_mfma_f32_16x16x32_bf16 v[32:35], v[164:167], v[216:219], v[32:35]
	v_add_f32_e32 v194, v194, v220
	v_add_f32_e32 v195, v195, v221
	v_mfma_f32_16x16x32_bf16 v[36:39], v[164:167], v[238:241], v[36:39]
	v_exp_f32_e32 v64, v64
	ds_read_b128 v[160:163], v201 offset:24576
	global_load_dwordx4 v[152:155], v196, s[6:7]
	s_waitcnt lgkmcnt(10)
	v_mfma_f32_16x16x32_bf16 v[76:79], v[168:171], v[116:119], v[76:79]
	v_exp_f32_e32 v68, v68
	v_mfma_f32_16x16x32_bf16 v[72:75], v[168:171], v[100:103], v[72:75]
	v_exp_f32_e32 v65, v65
	ds_read_b128 v[164:167], v210 offset:0
	global_load_dwordx4 v[156:159], v197, s[6:7]
	s_waitcnt lgkmcnt(9)
	v_mfma_f32_16x16x32_bf16 v[44:47], v[172:175], v[238:241], v[44:47]
	v_exp_f32_e32 v69, v69
	v_mfma_f32_16x16x32_bf16 v[40:43], v[172:175], v[216:219], v[40:43]
	v_exp_f32_e32 v66, v66
	ds_read_b128 v[168:171], v202 offset:24576
	s_waitcnt lgkmcnt(8)
	v_mfma_f32_16x16x32_bf16 v[72:75], v[176:179], v[104:107], v[72:75]
	v_exp_f32_e32 v70, v70
	v_mfma_f32_16x16x32_bf16 v[76:79], v[176:179], v[120:123], v[76:79]
	v_exp_f32_e32 v67, v67
	ds_read_b128 v[172:175], v210 offset:2048
	s_waitcnt lgkmcnt(7)
	v_mfma_f32_16x16x32_bf16 v[48:51], v[180:183], v[216:219], v[48:51]
	v_exp_f32_e32 v71, v71
	v_mfma_f32_16x16x32_bf16 v[52:55], v[180:183], v[238:241], v[52:55]
	v_add_f32_e32 v220, v64, v65
	ds_read_b128 v[176:179], v203 offset:24576
	s_waitcnt lgkmcnt(6)
	v_mfma_f32_16x16x32_bf16 v[76:79], v[230:233], v[124:127], v[76:79]
	v_add_f32_e32 v221, v68, v69
	v_mfma_f32_16x16x32_bf16 v[72:75], v[230:233], v[108:111], v[72:75]
	v_add_f32_e32 v220, v220, v66
	ds_read_b128 v[180:183], v210 offset:4096
	s_waitcnt lgkmcnt(6)
	v_mfma_f32_16x16x32_bf16 v[60:63], v[234:237], v[238:241], v[60:63]
	v_add_f32_e32 v221, v221, v70
	v_add_f32_e32 v220, v220, v67
	v_mfma_f32_16x16x32_bf16 v[56:59], v[234:237], v[216:219], v[56:59]
	v_add_f32_e32 v221, v221, v71
	ds_read_b128 v[230:233], v246 offset:24576
	s_waitcnt lgkmcnt(6)
	v_mfma_f32_16x16x32_bf16 v[80:83], v[160:163], v[96:99], 0
	v_exp_f32_e32 v72, v72
	v_mfma_f32_16x16x32_bf16 v[84:87], v[160:163], v[112:115], 0
	v_exp_f32_e32 v76, v76
	ds_read_b128 v[234:237], v210 offset:6144
	s_waitcnt lgkmcnt(6)
	v_mfma_f32_16x16x32_bf16 v[0:3], v[164:167], v[242:245], v[0:3]
	v_exp_f32_e32 v73, v73
	v_mfma_f32_16x16x32_bf16 v[4:7], v[164:167], v[204:207], v[4:7]
	v_exp_f32_e32 v77, v77
	ds_read_b128 v[160:163], v201 offset:28672
	s_waitcnt lgkmcnt(6)
	v_mfma_f32_16x16x32_bf16 v[84:87], v[168:171], v[116:119], v[84:87]
	v_exp_f32_e32 v74, v74
	v_mfma_f32_16x16x32_bf16 v[80:83], v[168:171], v[100:103], v[80:83]
	v_exp_f32_e32 v78, v78
	ds_read_b128 v[164:167], v210 offset:8192
	s_waitcnt lgkmcnt(6)
	v_mfma_f32_16x16x32_bf16 v[12:15], v[172:175], v[204:207], v[12:15]
	v_exp_f32_e32 v75, v75
	v_mfma_f32_16x16x32_bf16 v[8:11], v[172:175], v[242:245], v[8:11]
	v_exp_f32_e32 v79, v79
	ds_read_b128 v[168:171], v202 offset:28672
	s_waitcnt lgkmcnt(6)
	v_mfma_f32_16x16x32_bf16 v[80:83], v[176:179], v[104:107], v[80:83]
	v_add_f32_e32 v220, v220, v72
	v_add_f32_e32 v221, v221, v76
	v_mfma_f32_16x16x32_bf16 v[84:87], v[176:179], v[120:123], v[84:87]
	v_add_f32_e32 v220, v220, v73
	ds_read_b128 v[172:175], v210 offset:10240
	s_waitcnt lgkmcnt(6)
	v_mfma_f32_16x16x32_bf16 v[16:19], v[180:183], v[242:245], v[16:19]
	v_add_f32_e32 v221, v221, v77
	v_add_f32_e32 v220, v220, v74
	v_mfma_f32_16x16x32_bf16 v[20:23], v[180:183], v[204:207], v[20:23]
	v_add_f32_e32 v221, v221, v78
	ds_read_b128 v[176:179], v203 offset:28672
	s_waitcnt lgkmcnt(6)
	v_mfma_f32_16x16x32_bf16 v[84:87], v[230:233], v[124:127], v[84:87]
	v_add_f32_e32 v220, v220, v75
	v_add_f32_e32 v221, v221, v79
	v_mfma_f32_16x16x32_bf16 v[80:83], v[230:233], v[108:111], v[80:83]
	v_cvt_pk_bf16_f32 v216, v64, v65
	ds_read_b128 v[180:183], v210 offset:12288
	s_waitcnt lgkmcnt(6)
	v_mfma_f32_16x16x32_bf16 v[28:31], v[234:237], v[204:207], v[28:31]
	v_cvt_pk_bf16_f32 v217, v66, v67
	v_cvt_pk_bf16_f32 v238, v68, v69
	v_mfma_f32_16x16x32_bf16 v[24:27], v[234:237], v[242:245], v[24:27]
	v_cvt_pk_bf16_f32 v239, v70, v71
	ds_read_b128 v[230:233], v246 offset:28672
	s_waitcnt lgkmcnt(6)
	v_mfma_f32_16x16x32_bf16 v[88:91], v[160:163], v[96:99], 0
	v_exp_f32_e32 v80, v80
	v_mfma_f32_16x16x32_bf16 v[92:95], v[160:163], v[112:115], 0
	v_exp_f32_e32 v84, v84
	ds_read_b128 v[234:237], v210 offset:14336
	s_waitcnt lgkmcnt(6)
	v_mfma_f32_16x16x32_bf16 v[32:35], v[164:167], v[242:245], v[32:35]
	v_exp_f32_e32 v81, v81
	v_mfma_f32_16x16x32_bf16 v[36:39], v[164:167], v[204:207], v[36:39]
	v_exp_f32_e32 v85, v85
	ds_read_b128 v[160:163], v201 offset:32768
	s_waitcnt lgkmcnt(6)
	v_mfma_f32_16x16x32_bf16 v[92:95], v[168:171], v[116:119], v[92:95]
	v_exp_f32_e32 v82, v82
	v_mfma_f32_16x16x32_bf16 v[88:91], v[168:171], v[100:103], v[88:91]
	v_exp_f32_e32 v86, v86
	ds_read_b128 v[164:167], v209 offset:16384
	s_waitcnt lgkmcnt(6)
	v_mfma_f32_16x16x32_bf16 v[44:47], v[172:175], v[204:207], v[44:47]
	v_exp_f32_e32 v83, v83
	v_mfma_f32_16x16x32_bf16 v[40:43], v[172:175], v[242:245], v[40:43]
	v_exp_f32_e32 v87, v87
	ds_read_b128 v[168:171], v202 offset:32768
	s_waitcnt lgkmcnt(6)
	v_mfma_f32_16x16x32_bf16 v[88:91], v[176:179], v[104:107], v[88:91]
	v_add_f32_e32 v220, v220, v80
	v_add_f32_e32 v221, v221, v84
	v_mfma_f32_16x16x32_bf16 v[92:95], v[176:179], v[120:123], v[92:95]
	v_add_f32_e32 v220, v220, v81
	ds_read_b128 v[172:175], v209 offset:18432
	s_cmp_eq_u32 s100, 1
	s_cbranch_scc1 .Lattn_pax29
	s_setprio 1
	s_branch .Lattn_pbx29

.Lattn_pbx29:
	s_waitcnt lgkmcnt(6)
	v_mfma_f32_16x16x32_bf16 v[48:51], v[180:183], v[242:245], v[48:51]
	v_add_f32_e32 v221, v221, v85
	v_add_f32_e32 v220, v220, v82
	v_mfma_f32_16x16x32_bf16 v[52:55], v[180:183], v[204:207], v[52:55]
	v_add_f32_e32 v221, v221, v86
	ds_read_b128 v[176:179], v203 offset:32768
	s_waitcnt lgkmcnt(6)
	v_mfma_f32_16x16x32_bf16 v[92:95], v[230:233], v[124:127], v[92:95]
	v_add_f32_e32 v220, v220, v83
	v_add_f32_e32 v221, v221, v87
	v_mfma_f32_16x16x32_bf16 v[88:91], v[230:233], v[108:111], v[88:91]
	v_cvt_pk_bf16_f32 v218, v72, v73
	ds_read_b128 v[180:183], v209 offset:20480
	s_waitcnt lgkmcnt(6)
	v_mfma_f32_16x16x32_bf16 v[60:63], v[234:237], v[204:207], v[60:63]
	v_cvt_pk_bf16_f32 v219, v74, v75
	v_cvt_pk_bf16_f32 v240, v76, v77
	v_mfma_f32_16x16x32_bf16 v[56:59], v[234:237], v[242:245], v[56:59]
	v_cvt_pk_bf16_f32 v241, v78, v79
	ds_read_b128 v[230:233], v246 offset:32768
	s_waitcnt lgkmcnt(6)
	v_mfma_f32_16x16x32_bf16 v[64:67], v[160:163], v[96:99], 0
	v_exp_f32_e32 v88, v88
	v_mfma_f32_16x16x32_bf16 v[68:71], v[160:163], v[112:115], 0
	v_exp_f32_e32 v92, v92
	ds_read_b128 v[234:237], v209 offset:22528
	s_add_u32 s8, s16, 0x3bc00280
	s_addc_u32 s9, s17, 0
	s_add_u32 s6, s15, 0x23a60000
	s_addc_u32 s7, s14, 0
	s_waitcnt lgkmcnt(6)
	v_mfma_f32_16x16x32_bf16 v[0:3], v[164:167], v[216:219], v[0:3]
	v_cvt_pk_bf16_f32 v242, v80, v81
	v_mfma_f32_16x16x32_bf16 v[4:7], v[164:167], v[238:241], v[4:7]
	v_exp_f32_e32 v89, v89
	ds_read_b128 v[160:163], v201 offset:36864
	s_waitcnt vmcnt(4)
	ds_write_b128 v225, v[136:139] offset:0
	s_waitcnt lgkmcnt(7)
	v_mfma_f32_16x16x32_bf16 v[68:71], v[168:171], v[116:119], v[68:71]
	v_exp_f32_e32 v93, v93
	v_mfma_f32_16x16x32_bf16 v[64:67], v[168:171], v[100:103], v[64:67]
	v_cvt_pk_bf16_f32 v243, v82, v83
	ds_read_b128 v[164:167], v209 offset:24576
	ds_write_b128 v226, v[140:143] offset:0
	s_waitcnt lgkmcnt(8)
	v_mfma_f32_16x16x32_bf16 v[12:15], v[172:175], v[238:241], v[12:15]
	v_exp_f32_e32 v90, v90
	v_mfma_f32_16x16x32_bf16 v[8:11], v[172:175], v[216:219], v[8:11]
	v_exp_f32_e32 v94, v94
	ds_read_b128 v[168:171], v202 offset:36864
	ds_write_b64 v227, v[148:149] offset:49152
	s_waitcnt lgkmcnt(9)
	v_mfma_f32_16x16x32_bf16 v[64:67], v[176:179], v[104:107], v[64:67]
	v_cvt_pk_bf16_f32 v204, v84, v85
	v_mfma_f32_16x16x32_bf16 v[68:71], v[176:179], v[120:123], v[68:71]
	v_exp_f32_e32 v91, v91
	ds_read_b128 v[172:175], v209 offset:26624
	ds_write_b64 v228, v[150:151] offset:49152
	s_waitcnt lgkmcnt(10)
	v_mfma_f32_16x16x32_bf16 v[16:19], v[180:183], v[216:219], v[16:19]
	v_exp_f32_e32 v95, v95
	v_mfma_f32_16x16x32_bf16 v[20:23], v[180:183], v[238:241], v[20:23]
	v_cvt_pk_bf16_f32 v205, v86, v87
	v_add_f32_e32 v220, v220, v88
	ds_read_b128 v[176:179], v203 offset:36864
	ds_write_b64 v229, v[144:145] offset:49152
	s_waitcnt lgkmcnt(11)
	v_mfma_f32_16x16x32_bf16 v[68:71], v[230:233], v[124:127], v[68:71]
	v_add_f32_e32 v221, v221, v92
	v_add_f32_e32 v220, v220, v89
	v_mfma_f32_16x16x32_bf16 v[64:67], v[230:233], v[108:111], v[64:67]
	v_add_f32_e32 v221, v221, v93
	v_cvt_pk_bf16_f32 v244, v88, v89
	ds_read_b128 v[180:183], v209 offset:28672
	ds_write_b64 v184, v[146:147] offset:49152
	s_waitcnt lgkmcnt(12)
	v_mfma_f32_16x16x32_bf16 v[28:31], v[234:237], v[238:241], v[28:31]
	v_cvt_pk_bf16_f32 v245, v90, v91
	v_cvt_pk_bf16_f32 v206, v92, v93
	v_mfma_f32_16x16x32_bf16 v[24:27], v[234:237], v[216:219], v[24:27]
	v_cvt_pk_bf16_f32 v207, v94, v95
	ds_read_b128 v[230:233], v246 offset:36864
	global_load_dwordx4 v[148:151], v198, s[8:9]
	s_waitcnt lgkmcnt(12)
	v_mfma_f32_16x16x32_bf16 v[72:75], v[160:163], v[96:99], 0
	v_add_f32_e32 v220, v220, v90
	v_add_f32_e32 v221, v221, v94
	v_mfma_f32_16x16x32_bf16 v[76:79], v[160:163], v[112:115], 0
	v_add_f32_e32 v220, v220, v91
	v_add_f32_e32 v221, v221, v95
	ds_read_b128 v[234:237], v209 offset:30720
	global_load_dwordx4 v[144:147], v199, s[8:9]
	s_waitcnt lgkmcnt(11)
	v_mfma_f32_16x16x32_bf16 v[32:35], v[164:167], v[216:219], v[32:35]
	v_add_f32_e32 v194, v194, v220
	v_add_f32_e32 v195, v195, v221
	v_mfma_f32_16x16x32_bf16 v[36:39], v[164:167], v[238:241], v[36:39]
	v_exp_f32_e32 v64, v64
	ds_read_b128 v[160:163], v201 offset:40960
	global_load_dwordx4 v[136:139], v196, s[6:7]
	s_waitcnt lgkmcnt(10)
	v_mfma_f32_16x16x32_bf16 v[76:79], v[168:171], v[116:119], v[76:79]
	v_exp_f32_e32 v68, v68
	v_mfma_f32_16x16x32_bf16 v[72:75], v[168:171], v[100:103], v[72:75]
	v_exp_f32_e32 v65, v65
	ds_read_b128 v[164:167], v210 offset:16384
	global_load_dwordx4 v[140:143], v197, s[6:7]
	s_waitcnt lgkmcnt(9)
	v_mfma_f32_16x16x32_bf16 v[44:47], v[172:175], v[238:241], v[44:47]
	v_exp_f32_e32 v69, v69
	v_mfma_f32_16x16x32_bf16 v[40:43], v[172:175], v[216:219], v[40:43]
	v_exp_f32_e32 v66, v66
	ds_read_b128 v[168:171], v202 offset:40960
	s_waitcnt lgkmcnt(8)
	v_mfma_f32_16x16x32_bf16 v[72:75], v[176:179], v[104:107], v[72:75]
	v_exp_f32_e32 v70, v70
	v_mfma_f32_16x16x32_bf16 v[76:79], v[176:179], v[120:123], v[76:79]
	v_exp_f32_e32 v67, v67
	ds_read_b128 v[172:175], v210 offset:18432
	s_waitcnt lgkmcnt(7)
	v_mfma_f32_16x16x32_bf16 v[48:51], v[180:183], v[216:219], v[48:51]
	v_exp_f32_e32 v71, v71
	v_mfma_f32_16x16x32_bf16 v[52:55], v[180:183], v[238:241], v[52:55]
	v_add_f32_e32 v220, v64, v65
	ds_read_b128 v[176:179], v203 offset:40960
	s_waitcnt lgkmcnt(6)
	v_mfma_f32_16x16x32_bf16 v[76:79], v[230:233], v[124:127], v[76:79]
	v_add_f32_e32 v221, v68, v69
	v_mfma_f32_16x16x32_bf16 v[72:75], v[230:233], v[108:111], v[72:75]
	v_add_f32_e32 v220, v220, v66
	ds_read_b128 v[180:183], v210 offset:20480
	s_waitcnt lgkmcnt(6)
	v_mfma_f32_16x16x32_bf16 v[60:63], v[234:237], v[238:241], v[60:63]
	v_add_f32_e32 v221, v221, v70
	v_add_f32_e32 v220, v220, v67
	v_mfma_f32_16x16x32_bf16 v[56:59], v[234:237], v[216:219], v[56:59]
	v_add_f32_e32 v221, v221, v71
	ds_read_b128 v[230:233], v246 offset:40960
	s_waitcnt lgkmcnt(6)
	v_mfma_f32_16x16x32_bf16 v[80:83], v[160:163], v[96:99], 0
	v_exp_f32_e32 v72, v72
	v_mfma_f32_16x16x32_bf16 v[84:87], v[160:163], v[112:115], 0
	v_exp_f32_e32 v76, v76
	ds_read_b128 v[234:237], v210 offset:22528
	s_waitcnt lgkmcnt(6)
	v_mfma_f32_16x16x32_bf16 v[0:3], v[164:167], v[242:245], v[0:3]
	v_exp_f32_e32 v73, v73
	v_mfma_f32_16x16x32_bf16 v[4:7], v[164:167], v[204:207], v[4:7]
	v_exp_f32_e32 v77, v77
	ds_read_b128 v[160:163], v201 offset:45056
	s_waitcnt lgkmcnt(6)
	v_mfma_f32_16x16x32_bf16 v[84:87], v[168:171], v[116:119], v[84:87]
	v_exp_f32_e32 v74, v74
	v_mfma_f32_16x16x32_bf16 v[80:83], v[168:171], v[100:103], v[80:83]
	v_exp_f32_e32 v78, v78
	ds_read_b128 v[164:167], v210 offset:24576
	s_waitcnt lgkmcnt(6)
	v_mfma_f32_16x16x32_bf16 v[12:15], v[172:175], v[204:207], v[12:15]
	v_exp_f32_e32 v75, v75
	v_mfma_f32_16x16x32_bf16 v[8:11], v[172:175], v[242:245], v[8:11]
	v_exp_f32_e32 v79, v79
	ds_read_b128 v[168:171], v202 offset:45056
	s_waitcnt lgkmcnt(6)
	v_mfma_f32_16x16x32_bf16 v[80:83], v[176:179], v[104:107], v[80:83]
	v_add_f32_e32 v220, v220, v72
	v_add_f32_e32 v221, v221, v76
	v_mfma_f32_16x16x32_bf16 v[84:87], v[176:179], v[120:123], v[84:87]
	v_add_f32_e32 v220, v220, v73
	ds_read_b128 v[172:175], v210 offset:26624
	s_waitcnt lgkmcnt(6)
	v_mfma_f32_16x16x32_bf16 v[16:19], v[180:183], v[242:245], v[16:19]
	v_add_f32_e32 v221, v221, v77
	v_add_f32_e32 v220, v220, v74
	v_mfma_f32_16x16x32_bf16 v[20:23], v[180:183], v[204:207], v[20:23]
	v_add_f32_e32 v221, v221, v78
	ds_read_b128 v[176:179], v203 offset:45056
	s_waitcnt lgkmcnt(6)
	v_mfma_f32_16x16x32_bf16 v[84:87], v[230:233], v[124:127], v[84:87]
	v_add_f32_e32 v220, v220, v75
	v_add_f32_e32 v221, v221, v79
	v_mfma_f32_16x16x32_bf16 v[80:83], v[230:233], v[108:111], v[80:83]
	v_cvt_pk_bf16_f32 v216, v64, v65
	ds_read_b128 v[180:183], v210 offset:28672
	s_waitcnt lgkmcnt(6)
	v_mfma_f32_16x16x32_bf16 v[28:31], v[234:237], v[204:207], v[28:31]
	v_cvt_pk_bf16_f32 v217, v66, v67
	v_cvt_pk_bf16_f32 v238, v68, v69
	v_mfma_f32_16x16x32_bf16 v[24:27], v[234:237], v[242:245], v[24:27]
	v_cvt_pk_bf16_f32 v239, v70, v71
	ds_read_b128 v[230:233], v246 offset:45056
	s_waitcnt lgkmcnt(6)
	v_mfma_f32_16x16x32_bf16 v[88:91], v[160:163], v[96:99], 0
	v_exp_f32_e32 v80, v80
	v_mfma_f32_16x16x32_bf16 v[92:95], v[160:163], v[112:115], 0
	v_exp_f32_e32 v84, v84
	ds_read_b128 v[234:237], v210 offset:30720
	s_waitcnt lgkmcnt(6)
	v_mfma_f32_16x16x32_bf16 v[32:35], v[164:167], v[242:245], v[32:35]
	v_exp_f32_e32 v81, v81
	v_mfma_f32_16x16x32_bf16 v[36:39], v[164:167], v[204:207], v[36:39]
	v_exp_f32_e32 v85, v85
	s_waitcnt lgkmcnt(5)
	v_mfma_f32_16x16x32_bf16 v[92:95], v[168:171], v[116:119], v[92:95]
	v_exp_f32_e32 v82, v82
	v_mfma_f32_16x16x32_bf16 v[88:91], v[168:171], v[100:103], v[88:91]
	v_exp_f32_e32 v86, v86
	s_waitcnt lgkmcnt(4)
	v_mfma_f32_16x16x32_bf16 v[44:47], v[172:175], v[204:207], v[44:47]
	v_exp_f32_e32 v83, v83
	v_mfma_f32_16x16x32_bf16 v[40:43], v[172:175], v[242:245], v[40:43]
	v_exp_f32_e32 v87, v87
	s_waitcnt lgkmcnt(3)
	v_mfma_f32_16x16x32_bf16 v[88:91], v[176:179], v[104:107], v[88:91]
	v_add_f32_e32 v220, v220, v80
	v_add_f32_e32 v221, v221, v84
	v_mfma_f32_16x16x32_bf16 v[92:95], v[176:179], v[120:123], v[92:95]
	v_add_f32_e32 v220, v220, v81
	s_waitcnt lgkmcnt(0)
	s_barrier
	ds_read_b128 v[160:163], v201 offset:49152
	ds_read_b128 v[164:167], v209 offset:32768
	ds_read_b128 v[168:171], v202 offset:49152
	ds_read_b128 v[172:175], v209 offset:34816
	s_cmp_eq_u32 s100, 0
	s_cbranch_scc1 .Lattn_pax61
	s_setprio 1
	s_branch .Lattn_pbx61

.Lattn_pbx61:
	v_mfma_f32_16x16x32_bf16 v[48:51], v[180:183], v[242:245], v[48:51]
	v_add_f32_e32 v221, v221, v85
	v_add_f32_e32 v220, v220, v82
	v_mfma_f32_16x16x32_bf16 v[52:55], v[180:183], v[204:207], v[52:55]
	v_add_f32_e32 v221, v221, v86
	ds_read_b128 v[176:179], v203 offset:49152
	v_mfma_f32_16x16x32_bf16 v[92:95], v[230:233], v[124:127], v[92:95]
	v_add_f32_e32 v220, v220, v83
	v_add_f32_e32 v221, v221, v87
	v_mfma_f32_16x16x32_bf16 v[88:91], v[230:233], v[108:111], v[88:91]
	v_cvt_pk_bf16_f32 v218, v72, v73
	ds_read_b128 v[180:183], v209 offset:36864
	v_mfma_f32_16x16x32_bf16 v[60:63], v[234:237], v[204:207], v[60:63]
	v_cvt_pk_bf16_f32 v219, v74, v75
	v_cvt_pk_bf16_f32 v240, v76, v77
	v_mfma_f32_16x16x32_bf16 v[56:59], v[234:237], v[242:245], v[56:59]
	v_cvt_pk_bf16_f32 v241, v78, v79
	ds_read_b128 v[230:233], v246 offset:49152
	s_waitcnt lgkmcnt(6)
	v_mfma_f32_16x16x32_bf16 v[64:67], v[160:163], v[96:99], 0
	v_exp_f32_e32 v88, v88
	v_mfma_f32_16x16x32_bf16 v[68:71], v[160:163], v[112:115], 0
	v_exp_f32_e32 v92, v92
	ds_read_b128 v[234:237], v209 offset:38912
	s_add_u32 s8, s16, 0x3bc00300
	s_addc_u32 s9, s17, 0
	s_add_u32 s6, s15, 0x23a70000
	s_addc_u32 s7, s14, 0
	s_waitcnt lgkmcnt(6)
	v_mfma_f32_16x16x32_bf16 v[0:3], v[164:167], v[216:219], v[0:3]
	v_cvt_pk_bf16_f32 v242, v80, v81
	v_mfma_f32_16x16x32_bf16 v[4:7], v[164:167], v[238:241], v[4:7]
	v_exp_f32_e32 v89, v89
	ds_read_b128 v[160:163], v201 offset:53248
	s_waitcnt vmcnt(4)
	ds_write_b128 v225, v[152:155] offset:16384
	s_waitcnt lgkmcnt(7)
	v_mfma_f32_16x16x32_bf16 v[68:71], v[168:171], v[116:119], v[68:71]
	v_exp_f32_e32 v93, v93
	v_mfma_f32_16x16x32_bf16 v[64:67], v[168:171], v[100:103], v[64:67]
	v_cvt_pk_bf16_f32 v243, v82, v83
	ds_read_b128 v[164:167], v209 offset:40960
	ds_write_b128 v226, v[156:159] offset:16384
	s_waitcnt lgkmcnt(8)
	v_mfma_f32_16x16x32_bf16 v[12:15], v[172:175], v[238:241], v[12:15]
	v_exp_f32_e32 v90, v90
	v_mfma_f32_16x16x32_bf16 v[8:11], v[172:175], v[216:219], v[8:11]
	v_exp_f32_e32 v94, v94
	ds_read_b128 v[168:171], v202 offset:53248
	ds_write_b64 v227, v[132:133] offset:0
	s_waitcnt lgkmcnt(9)
	v_mfma_f32_16x16x32_bf16 v[64:67], v[176:179], v[104:107], v[64:67]
	v_cvt_pk_bf16_f32 v204, v84, v85
	v_mfma_f32_16x16x32_bf16 v[68:71], v[176:179], v[120:123], v[68:71]
	v_exp_f32_e32 v91, v91
	ds_read_b128 v[172:175], v209 offset:43008
	ds_write_b64 v228, v[134:135] offset:0
	s_waitcnt lgkmcnt(10)
	v_mfma_f32_16x16x32_bf16 v[16:19], v[180:183], v[216:219], v[16:19]
	v_exp_f32_e32 v95, v95
	v_mfma_f32_16x16x32_bf16 v[20:23], v[180:183], v[238:241], v[20:23]
	v_cvt_pk_bf16_f32 v205, v86, v87
	v_add_f32_e32 v220, v220, v88
	ds_read_b128 v[176:179], v203 offset:53248
	ds_write_b64 v229, v[128:129] offset:0
	s_waitcnt lgkmcnt(11)
	v_mfma_f32_16x16x32_bf16 v[68:71], v[230:233], v[124:127], v[68:71]
	v_add_f32_e32 v221, v221, v92
	v_add_f32_e32 v220, v220, v89
	v_mfma_f32_16x16x32_bf16 v[64:67], v[230:233], v[108:111], v[64:67]
	v_add_f32_e32 v221, v221, v93
	v_cvt_pk_bf16_f32 v244, v88, v89
	ds_read_b128 v[180:183], v209 offset:45056
	ds_write_b64 v184, v[130:131] offset:0
	s_waitcnt lgkmcnt(12)
	v_mfma_f32_16x16x32_bf16 v[28:31], v[234:237], v[238:241], v[28:31]
	v_cvt_pk_bf16_f32 v245, v90, v91
	v_cvt_pk_bf16_f32 v206, v92, v93
	v_mfma_f32_16x16x32_bf16 v[24:27], v[234:237], v[216:219], v[24:27]
	v_cvt_pk_bf16_f32 v207, v94, v95
	ds_read_b128 v[230:233], v246 offset:53248
	global_load_dwordx4 v[132:135], v198, s[8:9]
	s_waitcnt lgkmcnt(12)
	v_mfma_f32_16x16x32_bf16 v[72:75], v[160:163], v[96:99], 0
	v_add_f32_e32 v220, v220, v90
	v_add_f32_e32 v221, v221, v94
	v_mfma_f32_16x16x32_bf16 v[76:79], v[160:163], v[112:115], 0
	v_add_f32_e32 v220, v220, v91
	v_add_f32_e32 v221, v221, v95
	ds_read_b128 v[234:237], v209 offset:47104
	global_load_dwordx4 v[128:131], v199, s[8:9]
	s_waitcnt lgkmcnt(11)
	v_mfma_f32_16x16x32_bf16 v[32:35], v[164:167], v[216:219], v[32:35]
	v_add_f32_e32 v194, v194, v220
	v_add_f32_e32 v195, v195, v221
	v_mfma_f32_16x16x32_bf16 v[36:39], v[164:167], v[238:241], v[36:39]
	v_exp_f32_e32 v64, v64
	ds_read_b128 v[160:163], v201 offset:57344
	global_load_dwordx4 v[152:155], v196, s[6:7]
	s_waitcnt lgkmcnt(10)
	v_mfma_f32_16x16x32_bf16 v[76:79], v[168:171], v[116:119], v[76:79]
	v_exp_f32_e32 v68, v68
	v_mfma_f32_16x16x32_bf16 v[72:75], v[168:171], v[100:103], v[72:75]
	v_exp_f32_e32 v65, v65
	ds_read_b128 v[164:167], v210 offset:32768
	global_load_dwordx4 v[156:159], v197, s[6:7]
	s_waitcnt lgkmcnt(9)
	v_mfma_f32_16x16x32_bf16 v[44:47], v[172:175], v[238:241], v[44:47]
	v_exp_f32_e32 v69, v69
	v_mfma_f32_16x16x32_bf16 v[40:43], v[172:175], v[216:219], v[40:43]
	v_exp_f32_e32 v66, v66
	ds_read_b128 v[168:171], v202 offset:57344
	s_waitcnt lgkmcnt(8)
	v_mfma_f32_16x16x32_bf16 v[72:75], v[176:179], v[104:107], v[72:75]
	v_exp_f32_e32 v70, v70
	v_mfma_f32_16x16x32_bf16 v[76:79], v[176:179], v[120:123], v[76:79]
	v_exp_f32_e32 v67, v67
	ds_read_b128 v[172:175], v210 offset:34816
	s_waitcnt lgkmcnt(7)
	v_mfma_f32_16x16x32_bf16 v[48:51], v[180:183], v[216:219], v[48:51]
	v_exp_f32_e32 v71, v71
	v_mfma_f32_16x16x32_bf16 v[52:55], v[180:183], v[238:241], v[52:55]
	v_add_f32_e32 v220, v64, v65
	ds_read_b128 v[176:179], v203 offset:57344
	s_waitcnt lgkmcnt(6)
	v_mfma_f32_16x16x32_bf16 v[76:79], v[230:233], v[124:127], v[76:79]
	v_add_f32_e32 v221, v68, v69
	v_mfma_f32_16x16x32_bf16 v[72:75], v[230:233], v[108:111], v[72:75]
	v_add_f32_e32 v220, v220, v66
	ds_read_b128 v[180:183], v210 offset:36864
	s_waitcnt lgkmcnt(6)
	v_mfma_f32_16x16x32_bf16 v[60:63], v[234:237], v[238:241], v[60:63]
	v_add_f32_e32 v221, v221, v70
	v_add_f32_e32 v220, v220, v67
	v_mfma_f32_16x16x32_bf16 v[56:59], v[234:237], v[216:219], v[56:59]
	v_add_f32_e32 v221, v221, v71
	ds_read_b128 v[230:233], v246 offset:57344
	s_waitcnt lgkmcnt(6)
	v_mfma_f32_16x16x32_bf16 v[80:83], v[160:163], v[96:99], 0
	v_exp_f32_e32 v72, v72
	v_mfma_f32_16x16x32_bf16 v[84:87], v[160:163], v[112:115], 0
	v_exp_f32_e32 v76, v76
	ds_read_b128 v[234:237], v210 offset:38912
	s_waitcnt lgkmcnt(6)
	v_mfma_f32_16x16x32_bf16 v[0:3], v[164:167], v[242:245], v[0:3]
	v_exp_f32_e32 v73, v73
	v_mfma_f32_16x16x32_bf16 v[4:7], v[164:167], v[204:207], v[4:7]
	v_exp_f32_e32 v77, v77
	ds_read_b128 v[160:163], v201 offset:61440
	s_waitcnt lgkmcnt(6)
	v_mfma_f32_16x16x32_bf16 v[84:87], v[168:171], v[116:119], v[84:87]
	v_exp_f32_e32 v74, v74
	v_mfma_f32_16x16x32_bf16 v[80:83], v[168:171], v[100:103], v[80:83]
	v_exp_f32_e32 v78, v78
	ds_read_b128 v[164:167], v210 offset:40960
	s_waitcnt lgkmcnt(6)
	v_mfma_f32_16x16x32_bf16 v[12:15], v[172:175], v[204:207], v[12:15]
	v_exp_f32_e32 v75, v75
	v_mfma_f32_16x16x32_bf16 v[8:11], v[172:175], v[242:245], v[8:11]
	v_exp_f32_e32 v79, v79
	ds_read_b128 v[168:171], v202 offset:61440
	s_waitcnt lgkmcnt(6)
	v_mfma_f32_16x16x32_bf16 v[80:83], v[176:179], v[104:107], v[80:83]
	v_add_f32_e32 v220, v220, v72
	v_add_f32_e32 v221, v221, v76
	v_mfma_f32_16x16x32_bf16 v[84:87], v[176:179], v[120:123], v[84:87]
	v_add_f32_e32 v220, v220, v73
	ds_read_b128 v[172:175], v210 offset:43008
	s_waitcnt lgkmcnt(6)
	v_mfma_f32_16x16x32_bf16 v[16:19], v[180:183], v[242:245], v[16:19]
	v_add_f32_e32 v221, v221, v77
	v_add_f32_e32 v220, v220, v74
	v_mfma_f32_16x16x32_bf16 v[20:23], v[180:183], v[204:207], v[20:23]
	v_add_f32_e32 v221, v221, v78
	ds_read_b128 v[176:179], v203 offset:61440
	s_waitcnt lgkmcnt(6)
	v_mfma_f32_16x16x32_bf16 v[84:87], v[230:233], v[124:127], v[84:87]
	v_add_f32_e32 v220, v220, v75
	v_add_f32_e32 v221, v221, v79
	v_mfma_f32_16x16x32_bf16 v[80:83], v[230:233], v[108:111], v[80:83]
	v_cvt_pk_bf16_f32 v216, v64, v65
	ds_read_b128 v[180:183], v210 offset:45056
	s_waitcnt lgkmcnt(6)
	v_mfma_f32_16x16x32_bf16 v[28:31], v[234:237], v[204:207], v[28:31]
	v_cvt_pk_bf16_f32 v217, v66, v67
	v_cvt_pk_bf16_f32 v238, v68, v69
	v_mfma_f32_16x16x32_bf16 v[24:27], v[234:237], v[242:245], v[24:27]
	v_cvt_pk_bf16_f32 v239, v70, v71
	ds_read_b128 v[230:233], v246 offset:61440
	s_waitcnt lgkmcnt(6)
	v_mfma_f32_16x16x32_bf16 v[88:91], v[160:163], v[96:99], 0
	v_exp_f32_e32 v80, v80
	v_mfma_f32_16x16x32_bf16 v[92:95], v[160:163], v[112:115], 0
	v_exp_f32_e32 v84, v84
	ds_read_b128 v[234:237], v210 offset:47104
	s_waitcnt lgkmcnt(6)
	v_mfma_f32_16x16x32_bf16 v[32:35], v[164:167], v[242:245], v[32:35]
	v_exp_f32_e32 v81, v81
	v_mfma_f32_16x16x32_bf16 v[36:39], v[164:167], v[204:207], v[36:39]
	v_exp_f32_e32 v85, v85
	ds_read_b128 v[160:163], v201 offset:0
	s_waitcnt lgkmcnt(6)
	v_mfma_f32_16x16x32_bf16 v[92:95], v[168:171], v[116:119], v[92:95]
	v_exp_f32_e32 v82, v82
	v_mfma_f32_16x16x32_bf16 v[88:91], v[168:171], v[100:103], v[88:91]
	v_exp_f32_e32 v86, v86
	ds_read_b128 v[164:167], v209 offset:49152
	s_waitcnt lgkmcnt(6)
	v_mfma_f32_16x16x32_bf16 v[44:47], v[172:175], v[204:207], v[44:47]
	v_exp_f32_e32 v83, v83
	v_mfma_f32_16x16x32_bf16 v[40:43], v[172:175], v[242:245], v[40:43]
	v_exp_f32_e32 v87, v87
	ds_read_b128 v[168:171], v202 offset:0
	s_waitcnt lgkmcnt(6)
	v_mfma_f32_16x16x32_bf16 v[88:91], v[176:179], v[104:107], v[88:91]
	v_add_f32_e32 v220, v220, v80
	v_add_f32_e32 v221, v221, v84
	v_mfma_f32_16x16x32_bf16 v[92:95], v[176:179], v[120:123], v[92:95]
	v_add_f32_e32 v220, v220, v81
	ds_read_b128 v[172:175], v209 offset:51200
	s_cmp_eq_u32 s100, 1
	s_cbranch_scc1 .Lattn_pax93
	s_setprio 1
	s_branch .Lattn_pbx93

.Lattn_pbx93:
	s_waitcnt lgkmcnt(6)
	v_mfma_f32_16x16x32_bf16 v[48:51], v[180:183], v[242:245], v[48:51]
	v_add_f32_e32 v221, v221, v85
	v_add_f32_e32 v220, v220, v82
	v_mfma_f32_16x16x32_bf16 v[52:55], v[180:183], v[204:207], v[52:55]
	v_add_f32_e32 v221, v221, v86
	ds_read_b128 v[176:179], v203 offset:0
	s_waitcnt lgkmcnt(6)
	v_mfma_f32_16x16x32_bf16 v[92:95], v[230:233], v[124:127], v[92:95]
	v_add_f32_e32 v220, v220, v83
	v_add_f32_e32 v221, v221, v87
	v_mfma_f32_16x16x32_bf16 v[88:91], v[230:233], v[108:111], v[88:91]
	v_cvt_pk_bf16_f32 v218, v72, v73
	ds_read_b128 v[180:183], v209 offset:53248
	s_waitcnt lgkmcnt(6)
	v_mfma_f32_16x16x32_bf16 v[60:63], v[234:237], v[204:207], v[60:63]
	v_cvt_pk_bf16_f32 v219, v74, v75
	v_cvt_pk_bf16_f32 v240, v76, v77
	v_mfma_f32_16x16x32_bf16 v[56:59], v[234:237], v[242:245], v[56:59]
	v_cvt_pk_bf16_f32 v241, v78, v79
	ds_read_b128 v[230:233], v246 offset:0
	s_waitcnt lgkmcnt(6)
	v_mfma_f32_16x16x32_bf16 v[64:67], v[160:163], v[96:99], 0
	v_exp_f32_e32 v88, v88
	v_mfma_f32_16x16x32_bf16 v[68:71], v[160:163], v[112:115], 0
	v_exp_f32_e32 v92, v92
	ds_read_b128 v[234:237], v209 offset:55296
	s_add_u32 s8, s16, 0x3bc00380
	s_addc_u32 s9, s17, 0
	s_add_u32 s6, s15, 0x23a80000
	s_addc_u32 s7, s14, 0
	s_waitcnt lgkmcnt(6)
	v_mfma_f32_16x16x32_bf16 v[0:3], v[164:167], v[216:219], v[0:3]
	v_cvt_pk_bf16_f32 v242, v80, v81
	v_mfma_f32_16x16x32_bf16 v[4:7], v[164:167], v[238:241], v[4:7]
	v_exp_f32_e32 v89, v89
	ds_read_b128 v[160:163], v201 offset:4096
	s_waitcnt vmcnt(4)
	ds_write_b128 v225, v[136:139] offset:32768
	s_waitcnt lgkmcnt(7)
	v_mfma_f32_16x16x32_bf16 v[68:71], v[168:171], v[116:119], v[68:71]
	v_exp_f32_e32 v93, v93
	v_mfma_f32_16x16x32_bf16 v[64:67], v[168:171], v[100:103], v[64:67]
	v_cvt_pk_bf16_f32 v243, v82, v83
	ds_read_b128 v[164:167], v209 offset:57344
	ds_write_b128 v226, v[140:143] offset:32768
	s_waitcnt lgkmcnt(8)
	v_mfma_f32_16x16x32_bf16 v[12:15], v[172:175], v[238:241], v[12:15]
	v_exp_f32_e32 v90, v90
	v_mfma_f32_16x16x32_bf16 v[8:11], v[172:175], v[216:219], v[8:11]
	v_exp_f32_e32 v94, v94
	ds_read_b128 v[168:171], v202 offset:4096
	ds_write_b64 v227, v[148:149] offset:16384
	s_waitcnt lgkmcnt(9)
	v_mfma_f32_16x16x32_bf16 v[64:67], v[176:179], v[104:107], v[64:67]
	v_cvt_pk_bf16_f32 v204, v84, v85
	v_mfma_f32_16x16x32_bf16 v[68:71], v[176:179], v[120:123], v[68:71]
	v_exp_f32_e32 v91, v91
	ds_read_b128 v[172:175], v209 offset:59392
	ds_write_b64 v228, v[150:151] offset:16384
	s_waitcnt lgkmcnt(10)
	v_mfma_f32_16x16x32_bf16 v[16:19], v[180:183], v[216:219], v[16:19]
	v_exp_f32_e32 v95, v95
	v_mfma_f32_16x16x32_bf16 v[20:23], v[180:183], v[238:241], v[20:23]
	v_cvt_pk_bf16_f32 v205, v86, v87
	v_add_f32_e32 v220, v220, v88
	ds_read_b128 v[176:179], v203 offset:4096
	ds_write_b64 v229, v[144:145] offset:16384
	s_waitcnt lgkmcnt(11)
	v_mfma_f32_16x16x32_bf16 v[68:71], v[230:233], v[124:127], v[68:71]
	v_add_f32_e32 v221, v221, v92
	v_add_f32_e32 v220, v220, v89
	v_mfma_f32_16x16x32_bf16 v[64:67], v[230:233], v[108:111], v[64:67]
	v_add_f32_e32 v221, v221, v93
	v_cvt_pk_bf16_f32 v244, v88, v89
	ds_read_b128 v[180:183], v209 offset:61440
	ds_write_b64 v184, v[146:147] offset:16384
	s_waitcnt lgkmcnt(12)
	v_mfma_f32_16x16x32_bf16 v[28:31], v[234:237], v[238:241], v[28:31]
	v_cvt_pk_bf16_f32 v245, v90, v91
	v_cvt_pk_bf16_f32 v206, v92, v93
	v_mfma_f32_16x16x32_bf16 v[24:27], v[234:237], v[216:219], v[24:27]
	v_cvt_pk_bf16_f32 v207, v94, v95
	ds_read_b128 v[230:233], v246 offset:4096
	global_load_dwordx4 v[148:151], v198, s[8:9]
	s_waitcnt lgkmcnt(12)
	v_mfma_f32_16x16x32_bf16 v[72:75], v[160:163], v[96:99], 0
	v_add_f32_e32 v220, v220, v90
	v_add_f32_e32 v221, v221, v94
	v_mfma_f32_16x16x32_bf16 v[76:79], v[160:163], v[112:115], 0
	v_add_f32_e32 v220, v220, v91
	v_add_f32_e32 v221, v221, v95
	ds_read_b128 v[234:237], v209 offset:63488
	global_load_dwordx4 v[144:147], v199, s[8:9]
	s_waitcnt lgkmcnt(11)
	v_mfma_f32_16x16x32_bf16 v[32:35], v[164:167], v[216:219], v[32:35]
	v_add_f32_e32 v194, v194, v220
	v_add_f32_e32 v195, v195, v221
	v_mfma_f32_16x16x32_bf16 v[36:39], v[164:167], v[238:241], v[36:39]
	v_exp_f32_e32 v64, v64
	ds_read_b128 v[160:163], v201 offset:8192
	global_load_dwordx4 v[136:139], v196, s[6:7]
	s_waitcnt lgkmcnt(10)
	v_mfma_f32_16x16x32_bf16 v[76:79], v[168:171], v[116:119], v[76:79]
	v_exp_f32_e32 v68, v68
	v_mfma_f32_16x16x32_bf16 v[72:75], v[168:171], v[100:103], v[72:75]
	v_exp_f32_e32 v65, v65
	ds_read_b128 v[164:167], v210 offset:49152
	global_load_dwordx4 v[140:143], v197, s[6:7]
	s_waitcnt lgkmcnt(9)
	v_mfma_f32_16x16x32_bf16 v[44:47], v[172:175], v[238:241], v[44:47]
	v_exp_f32_e32 v69, v69
	v_mfma_f32_16x16x32_bf16 v[40:43], v[172:175], v[216:219], v[40:43]
	v_exp_f32_e32 v66, v66
	ds_read_b128 v[168:171], v202 offset:8192
	s_waitcnt lgkmcnt(8)
	v_mfma_f32_16x16x32_bf16 v[72:75], v[176:179], v[104:107], v[72:75]
	v_exp_f32_e32 v70, v70
	v_mfma_f32_16x16x32_bf16 v[76:79], v[176:179], v[120:123], v[76:79]
	v_exp_f32_e32 v67, v67
	ds_read_b128 v[172:175], v210 offset:51200
	s_waitcnt lgkmcnt(7)
	v_mfma_f32_16x16x32_bf16 v[48:51], v[180:183], v[216:219], v[48:51]
	v_exp_f32_e32 v71, v71
	v_mfma_f32_16x16x32_bf16 v[52:55], v[180:183], v[238:241], v[52:55]
	v_add_f32_e32 v220, v64, v65
	ds_read_b128 v[176:179], v203 offset:8192
	s_waitcnt lgkmcnt(6)
	v_mfma_f32_16x16x32_bf16 v[76:79], v[230:233], v[124:127], v[76:79]
	v_add_f32_e32 v221, v68, v69
	v_mfma_f32_16x16x32_bf16 v[72:75], v[230:233], v[108:111], v[72:75]
	v_add_f32_e32 v220, v220, v66
	ds_read_b128 v[180:183], v210 offset:53248
	s_waitcnt lgkmcnt(6)
	v_mfma_f32_16x16x32_bf16 v[60:63], v[234:237], v[238:241], v[60:63]
	v_add_f32_e32 v221, v221, v70
	v_add_f32_e32 v220, v220, v67
	v_mfma_f32_16x16x32_bf16 v[56:59], v[234:237], v[216:219], v[56:59]
	v_add_f32_e32 v221, v221, v71
	ds_read_b128 v[230:233], v246 offset:8192
	s_waitcnt lgkmcnt(6)
	v_mfma_f32_16x16x32_bf16 v[80:83], v[160:163], v[96:99], 0
	v_exp_f32_e32 v72, v72
	v_mfma_f32_16x16x32_bf16 v[84:87], v[160:163], v[112:115], 0
	v_exp_f32_e32 v76, v76
	ds_read_b128 v[234:237], v210 offset:55296
	s_waitcnt lgkmcnt(6)
	v_mfma_f32_16x16x32_bf16 v[0:3], v[164:167], v[242:245], v[0:3]
	v_exp_f32_e32 v73, v73
	v_mfma_f32_16x16x32_bf16 v[4:7], v[164:167], v[204:207], v[4:7]
	v_exp_f32_e32 v77, v77
	ds_read_b128 v[160:163], v201 offset:12288
	s_waitcnt lgkmcnt(6)
	v_mfma_f32_16x16x32_bf16 v[84:87], v[168:171], v[116:119], v[84:87]
	v_exp_f32_e32 v74, v74
	v_mfma_f32_16x16x32_bf16 v[80:83], v[168:171], v[100:103], v[80:83]
	v_exp_f32_e32 v78, v78
	ds_read_b128 v[164:167], v210 offset:57344
	s_waitcnt lgkmcnt(6)
	v_mfma_f32_16x16x32_bf16 v[12:15], v[172:175], v[204:207], v[12:15]
	v_exp_f32_e32 v75, v75
	v_mfma_f32_16x16x32_bf16 v[8:11], v[172:175], v[242:245], v[8:11]
	v_exp_f32_e32 v79, v79
	ds_read_b128 v[168:171], v202 offset:12288
	s_waitcnt lgkmcnt(6)
	v_mfma_f32_16x16x32_bf16 v[80:83], v[176:179], v[104:107], v[80:83]
	v_add_f32_e32 v220, v220, v72
	v_add_f32_e32 v221, v221, v76
	v_mfma_f32_16x16x32_bf16 v[84:87], v[176:179], v[120:123], v[84:87]
	v_add_f32_e32 v220, v220, v73
	ds_read_b128 v[172:175], v210 offset:59392
	s_add_u32 s10, s10, 0x200
	s_addc_u32 s11, s11, 0
	s_add_u32 s12, s12, 0x40000
	s_addc_u32 s13, s13, 0
	s_add_i32 s4, s4, 4
	s_cmpk_lt_u32 s4, 0x104
	s_cselect_b64 s[6:7], -1, 0
	s_and_b64 s[6:7], s[0:1], s[6:7]
	s_and_b64 vcc, exec, s[6:7]
	s_waitcnt lgkmcnt(6)
	v_mfma_f32_16x16x32_bf16 v[16:19], v[180:183], v[242:245], v[16:19]
	v_add_f32_e32 v221, v221, v77
	v_add_f32_e32 v220, v220, v74
	v_mfma_f32_16x16x32_bf16 v[20:23], v[180:183], v[204:207], v[20:23]
	v_add_f32_e32 v221, v221, v78
	ds_read_b128 v[176:179], v203 offset:12288
	s_waitcnt lgkmcnt(6)
	v_mfma_f32_16x16x32_bf16 v[84:87], v[230:233], v[124:127], v[84:87]
	v_add_f32_e32 v220, v220, v75
	v_add_f32_e32 v221, v221, v79
	v_mfma_f32_16x16x32_bf16 v[80:83], v[230:233], v[108:111], v[80:83]
	v_cvt_pk_bf16_f32 v216, v64, v65
	ds_read_b128 v[180:183], v210 offset:61440
	s_waitcnt lgkmcnt(6)
	v_mfma_f32_16x16x32_bf16 v[28:31], v[234:237], v[204:207], v[28:31]
	v_cvt_pk_bf16_f32 v217, v66, v67
	v_cvt_pk_bf16_f32 v238, v68, v69
	v_mfma_f32_16x16x32_bf16 v[24:27], v[234:237], v[242:245], v[24:27]
	v_cvt_pk_bf16_f32 v239, v70, v71
	ds_read_b128 v[230:233], v246 offset:12288
	s_waitcnt lgkmcnt(6)
	v_mfma_f32_16x16x32_bf16 v[88:91], v[160:163], v[96:99], 0
	v_exp_f32_e32 v80, v80
	v_mfma_f32_16x16x32_bf16 v[92:95], v[160:163], v[112:115], 0
	v_exp_f32_e32 v84, v84
	ds_read_b128 v[234:237], v210 offset:63488
	s_waitcnt lgkmcnt(6)
	v_mfma_f32_16x16x32_bf16 v[32:35], v[164:167], v[242:245], v[32:35]
	v_exp_f32_e32 v81, v81
	v_mfma_f32_16x16x32_bf16 v[36:39], v[164:167], v[204:207], v[36:39]
	v_exp_f32_e32 v85, v85
	s_waitcnt lgkmcnt(5)
	v_mfma_f32_16x16x32_bf16 v[92:95], v[168:171], v[116:119], v[92:95]
	v_exp_f32_e32 v82, v82
	v_mfma_f32_16x16x32_bf16 v[88:91], v[168:171], v[100:103], v[88:91]
	v_exp_f32_e32 v86, v86
	s_waitcnt lgkmcnt(4)
	v_mfma_f32_16x16x32_bf16 v[44:47], v[172:175], v[204:207], v[44:47]
	v_exp_f32_e32 v83, v83
	v_mfma_f32_16x16x32_bf16 v[40:43], v[172:175], v[242:245], v[40:43]
	v_exp_f32_e32 v87, v87
	s_waitcnt lgkmcnt(3)
	v_mfma_f32_16x16x32_bf16 v[88:91], v[176:179], v[104:107], v[88:91]
	v_add_f32_e32 v220, v220, v80
	v_add_f32_e32 v221, v221, v84
	v_mfma_f32_16x16x32_bf16 v[92:95], v[176:179], v[120:123], v[92:95]
	v_add_f32_e32 v220, v220, v81
	s_waitcnt lgkmcnt(0)
	s_barrier
	ds_read_b128 v[160:163], v201 offset:16384
	ds_read_b128 v[164:167], v209 offset:0
	ds_read_b128 v[168:171], v202 offset:16384
	ds_read_b128 v[172:175], v209 offset:2048
	s_cmp_eq_u32 s100, 0
	s_cbranch_scc1 .Lattn_pax125
	s_setprio 1
	s_branch .Lattn_pbx125

.Lattn_pbx125:
	v_mfma_f32_16x16x32_bf16 v[48:51], v[180:183], v[242:245], v[48:51]
	v_add_f32_e32 v221, v221, v85
	v_add_f32_e32 v220, v220, v82
	v_mfma_f32_16x16x32_bf16 v[52:55], v[180:183], v[204:207], v[52:55]
	v_add_f32_e32 v221, v221, v86
	ds_read_b128 v[176:179], v203 offset:16384
	v_mfma_f32_16x16x32_bf16 v[92:95], v[230:233], v[124:127], v[92:95]
	v_add_f32_e32 v220, v220, v83
	v_add_f32_e32 v221, v221, v87
	v_mfma_f32_16x16x32_bf16 v[88:91], v[230:233], v[108:111], v[88:91]
	v_cvt_pk_bf16_f32 v218, v72, v73
	ds_read_b128 v[180:183], v209 offset:4096
	v_mfma_f32_16x16x32_bf16 v[60:63], v[234:237], v[204:207], v[60:63]
	v_cvt_pk_bf16_f32 v219, v74, v75
	v_cvt_pk_bf16_f32 v240, v76, v77
	v_mfma_f32_16x16x32_bf16 v[56:59], v[234:237], v[242:245], v[56:59]
	v_cvt_pk_bf16_f32 v241, v78, v79
	ds_read_b128 v[230:233], v246 offset:16384
	s_cbranch_vccnz .LBB0_734
	s_setprio 0
	s_waitcnt vmcnt(0)
	s_nop 7
	s_nop 7
	ds_swizzle_b32 v64, v194 offset:swizzle(SWAP,16)
	s_waitcnt lgkmcnt(0)
	v_add_f32_e32 v194, v194, v64
	v_mov_b32_e32 v65, v194
	s_nop 1
	v_permlane32_swap_b32_e32 v194, v65
	v_add_f32_e32 v194, v194, v65
	s_nop 0
	v_rcp_f32_e32 v66, v194
	ds_swizzle_b32 v64, v195 offset:swizzle(SWAP,16)
	s_waitcnt lgkmcnt(0)
	v_add_f32_e32 v195, v195, v64
	v_mov_b32_e32 v65, v195
	s_nop 1
	v_permlane32_swap_b32_e32 v195, v65
	v_add_f32_e32 v195, v195, v65
	s_nop 0
	v_rcp_f32_e32 v67, v195
	v_readlane_b32 s100, v250, 8
	v_mbcnt_lo_u32_b32 v68, -1, 0
	v_mbcnt_hi_u32_b32 v68, -1, v68
	v_and_b32_e32 v69, 15, v68
	v_lshrrev_b32_e32 v70, 4, v68
	s_lshr_b32 s101, s100, 1
	v_add_u32_e32 v69, s101, v69
	v_lshlrev_b32_e32 v69, 12, v69
	v_and_b32_e32 v71, 1, v70
	v_lshlrev_b32_e32 v71, 5, v71
	v_and_b32_e32 v70, 2, v70
	v_lshl_add_u32 v71, v70, 3, v71
	v_add_u32_e32 v70, v69, v71
	v_add_u32_e32 v71, 0x10000, v70
	v_mul_f32_e32 v0, v0, v66
	v_mul_f32_e32 v1, v1, v66
	v_mul_f32_e32 v2, v2, v66
	v_mul_f32_e32 v3, v3, v66
	v_mul_f32_e32 v8, v8, v66
	v_mul_f32_e32 v9, v9, v66
	v_mul_f32_e32 v10, v10, v66
	v_mul_f32_e32 v11, v11, v66
	v_cvt_pk_bf16_f32 v72, v0, v1
	v_cvt_pk_bf16_f32 v73, v2, v3
	v_cvt_pk_bf16_f32 v74, v8, v9
	v_cvt_pk_bf16_f32 v75, v10, v11
	s_nop 1
	v_permlane16_swap_b32_e32 v72, v74
	v_permlane16_swap_b32_e32 v73, v75
	s_nop 1
	global_store_dwordx4 v70, v[72:75], s[58:59] offset:0
	v_mul_f32_e32 v16, v16, v66
	v_mul_f32_e32 v17, v17, v66
	v_mul_f32_e32 v18, v18, v66
	v_mul_f32_e32 v19, v19, v66
	v_mul_f32_e32 v24, v24, v66
	v_mul_f32_e32 v25, v25, v66
	v_mul_f32_e32 v26, v26, v66
	v_mul_f32_e32 v27, v27, v66
	v_cvt_pk_bf16_f32 v76, v16, v17
	v_cvt_pk_bf16_f32 v77, v18, v19
	v_cvt_pk_bf16_f32 v78, v24, v25
	v_cvt_pk_bf16_f32 v79, v26, v27
	s_nop 1
	v_permlane16_swap_b32_e32 v76, v78
	v_permlane16_swap_b32_e32 v77, v79
	s_nop 1
	global_store_dwordx4 v70, v[76:79], s[58:59] offset:64
	v_mul_f32_e32 v32, v32, v66
	v_mul_f32_e32 v33, v33, v66
	v_mul_f32_e32 v34, v34, v66
	v_mul_f32_e32 v35, v35, v66
	v_mul_f32_e32 v40, v40, v66
	v_mul_f32_e32 v41, v41, v66
	v_mul_f32_e32 v42, v42, v66
	v_mul_f32_e32 v43, v43, v66
	v_cvt_pk_bf16_f32 v80, v32, v33
	v_cvt_pk_bf16_f32 v81, v34, v35
	v_cvt_pk_bf16_f32 v82, v40, v41
	v_cvt_pk_bf16_f32 v83, v42, v43
	s_nop 1
	v_permlane16_swap_b32_e32 v80, v82
	v_permlane16_swap_b32_e32 v81, v83
	s_nop 1
	global_store_dwordx4 v70, v[80:83], s[58:59] offset:128
	v_mul_f32_e32 v48, v48, v66
	v_mul_f32_e32 v49, v49, v66
	v_mul_f32_e32 v50, v50, v66
	v_mul_f32_e32 v51, v51, v66
	v_mul_f32_e32 v56, v56, v66
	v_mul_f32_e32 v57, v57, v66
	v_mul_f32_e32 v58, v58, v66
	v_mul_f32_e32 v59, v59, v66
	v_cvt_pk_bf16_f32 v84, v48, v49
	v_cvt_pk_bf16_f32 v85, v50, v51
	v_cvt_pk_bf16_f32 v86, v56, v57
	v_cvt_pk_bf16_f32 v87, v58, v59
	s_nop 1
	v_permlane16_swap_b32_e32 v84, v86
	v_permlane16_swap_b32_e32 v85, v87
	s_nop 1
	global_store_dwordx4 v70, v[84:87], s[58:59] offset:192
	v_mul_f32_e32 v4, v4, v67
	v_mul_f32_e32 v5, v5, v67
	v_mul_f32_e32 v6, v6, v67
	v_mul_f32_e32 v7, v7, v67
	v_mul_f32_e32 v12, v12, v67
	v_mul_f32_e32 v13, v13, v67
	v_mul_f32_e32 v14, v14, v67
	v_mul_f32_e32 v15, v15, v67
	v_cvt_pk_bf16_f32 v88, v4, v5
	v_cvt_pk_bf16_f32 v89, v6, v7
	v_cvt_pk_bf16_f32 v90, v12, v13
	v_cvt_pk_bf16_f32 v91, v14, v15
	s_nop 1
	v_permlane16_swap_b32_e32 v88, v90
	v_permlane16_swap_b32_e32 v89, v91
	s_nop 1
	global_store_dwordx4 v71, v[88:91], s[58:59] offset:0
	v_mul_f32_e32 v20, v20, v67
	v_mul_f32_e32 v21, v21, v67
	v_mul_f32_e32 v22, v22, v67
	v_mul_f32_e32 v23, v23, v67
	v_mul_f32_e32 v28, v28, v67
	v_mul_f32_e32 v29, v29, v67
	v_mul_f32_e32 v30, v30, v67
	v_mul_f32_e32 v31, v31, v67
	v_cvt_pk_bf16_f32 v92, v20, v21
	v_cvt_pk_bf16_f32 v93, v22, v23
	v_cvt_pk_bf16_f32 v94, v28, v29
	v_cvt_pk_bf16_f32 v95, v30, v31
	s_nop 1
	v_permlane16_swap_b32_e32 v92, v94
	v_permlane16_swap_b32_e32 v93, v95
	s_nop 1
	global_store_dwordx4 v71, v[92:95], s[58:59] offset:64
	v_mul_f32_e32 v36, v36, v67
	v_mul_f32_e32 v37, v37, v67
	v_mul_f32_e32 v38, v38, v67
	v_mul_f32_e32 v39, v39, v67
	v_mul_f32_e32 v44, v44, v67
	v_mul_f32_e32 v45, v45, v67
	v_mul_f32_e32 v46, v46, v67
	v_mul_f32_e32 v47, v47, v67
	v_cvt_pk_bf16_f32 v72, v36, v37
	v_cvt_pk_bf16_f32 v73, v38, v39
	v_cvt_pk_bf16_f32 v74, v44, v45
	v_cvt_pk_bf16_f32 v75, v46, v47
	s_nop 1
	v_permlane16_swap_b32_e32 v72, v74
	v_permlane16_swap_b32_e32 v73, v75
	s_nop 1
	global_store_dwordx4 v71, v[72:75], s[58:59] offset:128
	v_mul_f32_e32 v52, v52, v67
	v_mul_f32_e32 v53, v53, v67
	v_mul_f32_e32 v54, v54, v67
	v_mul_f32_e32 v55, v55, v67
	v_mul_f32_e32 v60, v60, v67
	v_mul_f32_e32 v61, v61, v67
	v_mul_f32_e32 v62, v62, v67
	v_mul_f32_e32 v63, v63, v67
	v_cvt_pk_bf16_f32 v76, v52, v53
	v_cvt_pk_bf16_f32 v77, v54, v55
	v_cvt_pk_bf16_f32 v78, v60, v61
	v_cvt_pk_bf16_f32 v79, v62, v63
	s_nop 1
	v_permlane16_swap_b32_e32 v76, v78
	v_permlane16_swap_b32_e32 v77, v79
	s_nop 1
	global_store_dwordx4 v71, v[76:79], s[58:59] offset:192
	s_barrier
